# norm2+router: hand-scheduled router-logit MFMA section, weight fragments streamed through an 18-slot register ring with counted vmcnt
# speedup vs baseline: 1.0273x; 1.0128x over previous
; #define LAS __attribute__((address_space(3)))
; __device__ __forceinline__ unsigned cvt_pk_bf16(float lo, float hi) { const bf16x2_t r = __builtin_convertvector((f32x2_t){lo, hi}, bf16x2_t); return __builtin_bit_cast(unsigned, r); }
; template <int MODE>
; __device__ __forceinline__ void norm_phase(const MkArgs& a, LAS unsigned char* lds, const int l, const int wv) {
;     ...
;         __syncthreads();
;         float tot = 0.f;
; #pragma unroll
;         for (int i = 0; i < 8; ++i) tot += ssp[i * 16 + r];
;         const float rstd = 1.0f / sqrtf(tot * (1.0f / DM) + EPSV);
; #pragma unroll
;         for (int j = 0; j < 8; ++j) {
;             const int k = 256 * w + 32 * j + 8 * q;
;             const f32x4 g0 = *(const LAS f32x4*)&tabA[k], g1 = *(const LAS f32x4*)&tabA[k + 4];
;             float gg[8] = {g0[0], g0[1], g0[2], g0[3], g1[0], g1[1], g1[2], g1[3]};
;             if constexpr (MODE != 3) {
;                 const f32x4 s0 = *(const LAS f32x4*)&tabB[k], s1 = *(const LAS f32x4*)&tabB[k + 4];
;                 const float sv[8] = {s0[0], s0[1], s0[2], s0[3], s1[0], s1[1], s1[2], s1[3]};
; #pragma unroll
;                 for (int i = 0; i < 8; ++i) xv[8 * j + i] = (xv[8 * j + i] * rstd) * gg[i] + sv[i];
;                 u32x4 o; o[0] = cvt_pk_bf16(xv[8 * j + 0], xv[8 * j + 1]); o[1] = cvt_pk_bf16(xv[8 * j + 2], xv[8 * j + 3]);
;                 o[2] = cvt_pk_bf16(xv[8 * j + 4], xv[8 * j + 5]); o[3] = cvt_pk_bf16(xv[8 * j + 6], xv[8 * j + 7]);
;                 *(u32x4*)(hb + (size_t)t * DM + k) = o;
.LBB0_901:
	s_or_b64 exec, exec, s[12:13]
	s_waitcnt lgkmcnt(0)
	s_barrier
	ds_read2_b32 v[84:85], v151 offset1:16
	ds_read2_b32 v[86:87], v151 offset0:32 offset1:48
	ds_read2_b32 v[88:89], v151 offset0:64 offset1:80
	s_mov_b32 s12, 0xf800000
	v_lshlrev_b64 v[82:83], 12, v[82:83]
	s_waitcnt lgkmcnt(2)
	v_add_f32_e32 v76, 0, v84
	v_add_f32_e32 v76, v76, v85
	ds_read2_b32 v[84:85], v151 offset0:96 offset1:112
	s_waitcnt lgkmcnt(2)
	v_add_f32_e32 v76, v76, v86
	v_add_f32_e32 v76, v76, v87
	s_waitcnt lgkmcnt(1)
	v_add_f32_e32 v76, v76, v88
	v_add_f32_e32 v76, v76, v89
	s_waitcnt lgkmcnt(0)
	v_add_f32_e32 v76, v76, v84
	v_add_f32_e32 v76, v76, v85
	v_fmamk_f32 v76, v76, 0x3a000000, v154
	v_mul_f32_e32 v84, 0x4f800000, v76
	v_cmp_gt_f32_e32 vcc, s12, v76
	v_lshl_add_u64 v[172:173], v[70:71], 0, v[82:83]
	s_nop 0
	v_cndmask_b32_e32 v76, v76, v84, vcc
	v_sqrt_f32_e32 v84, v76
	s_nop 0
	v_add_u32_e32 v85, -1, v84
	v_fma_f32 v86, -v85, v84, v76
	v_cmp_ge_f32_e64 s[12:13], 0, v86
	v_add_u32_e32 v86, 1, v84
	s_nop 0
	v_cndmask_b32_e64 v85, v84, v85, s[12:13]
	v_fma_f32 v84, -v86, v84, v76
	v_cmp_lt_f32_e64 s[12:13], 0, v84
	s_nop 1
	v_cndmask_b32_e64 v84, v85, v86, s[12:13]
	v_mul_f32_e32 v85, 0x37800000, v84
	v_cndmask_b32_e32 v84, v84, v85, vcc
	v_cmp_class_f32_e32 vcc, v76, v155
	s_nop 1
	v_cndmask_b32_e32 v76, v84, v76, vcc
	v_div_scale_f32 v84, s[12:13], v76, v76, 1.0
	v_rcp_f32_e32 v85, v84
	s_movk_i32 s12, 0x2000
	v_fma_f32 v86, -v84, v85, 1.0
	v_fmac_f32_e32 v85, v86, v85
	v_div_scale_f32 v86, vcc, 1.0, v76, 1.0
	v_mul_f32_e32 v87, v86, v85
	v_fma_f32 v88, -v84, v87, v86
	v_fmac_f32_e32 v87, v88, v85
	v_fma_f32 v84, -v84, v87, v86
	v_div_fmas_f32 v84, v84, v85, v87
	v_div_fixup_f32 v76, v84, v76, 1.0
	ds_read_b128 v[84:87], v65
	ds_read_b128 v[88:91], v118
	ds_read_b128 v[92:95], v117
	ds_read_b128 v[96:99], v119
	v_pk_mul_f32 v[60:61], v[60:61], v[76:77] op_sel_hi:[1,0]
	v_pk_mul_f32 v[44:45], v[44:45], v[76:77] op_sel_hi:[1,0]
	v_pk_mul_f32 v[56:57], v[56:57], v[76:77] op_sel_hi:[1,0]
	s_waitcnt lgkmcnt(2)
	v_pk_fma_f32 v[108:109], v[84:85], v[60:61], v[88:89]
	v_pk_mul_f32 v[60:61], v[62:63], v[76:77] op_sel_hi:[1,0]
	s_waitcnt lgkmcnt(0)
	v_pk_fma_f32 v[106:107], v[92:93], v[44:45], v[96:97]
	v_pk_mul_f32 v[44:45], v[46:47], v[76:77] op_sel_hi:[1,0]
	v_pk_fma_f32 v[112:113], v[86:87], v[60:61], v[90:91]
	v_pk_fma_f32 v[110:111], v[94:95], v[44:45], v[98:99]
	v_cvt_pk_bf16_f32 v44, v108, v109
	v_cvt_pk_bf16_f32 v45, v112, v113
	v_cvt_pk_bf16_f32 v46, v106, v107
	v_cvt_pk_bf16_f32 v47, v110, v111
	ds_read_b128 v[60:63], v120
	ds_read_b128 v[82:85], v122
	global_store_dwordx4 v[172:173], v[44:47], off
	ds_read_b128 v[86:89], v121
	ds_read_b128 v[90:93], v123
	v_pk_mul_f32 v[24:25], v[24:25], v[76:77] op_sel_hi:[1,0]
	v_pk_mul_f32 v[52:53], v[52:53], v[76:77] op_sel_hi:[1,0]
	s_waitcnt lgkmcnt(2)
	v_pk_fma_f32 v[98:99], v[56:57], v[60:61], v[82:83]
	v_pk_mul_f32 v[56:57], v[58:59], v[76:77] op_sel_hi:[1,0]
	s_waitcnt lgkmcnt(0)
	v_pk_fma_f32 v[100:101], v[24:25], v[86:87], v[90:91]
	v_pk_mul_f32 v[24:25], v[26:27], v[76:77] op_sel_hi:[1,0]
	v_pk_fma_f32 v[102:103], v[56:57], v[62:63], v[84:85]
	v_pk_fma_f32 v[104:105], v[24:25], v[88:89], v[92:93]
	v_cvt_pk_bf16_f32 v24, v98, v99
	v_cvt_pk_bf16_f32 v25, v102, v103
	v_cvt_pk_bf16_f32 v26, v100, v101
	v_cvt_pk_bf16_f32 v27, v104, v105
	ds_read_b128 v[56:59], v124
	ds_read_b128 v[60:63], v126
	global_store_dwordx4 v[172:173], v[24:27], off offset:64
	ds_read_b128 v[82:85], v125
	ds_read_b128 v[86:89], v127
	v_pk_mul_f32 v[4:5], v[4:5], v[76:77] op_sel_hi:[1,0]
	v_pk_mul_f32 v[48:49], v[48:49], v[76:77] op_sel_hi:[1,0]
	s_waitcnt lgkmcnt(2)
	v_pk_fma_f32 v[90:91], v[52:53], v[56:57], v[60:61]
	v_pk_mul_f32 v[52:53], v[54:55], v[76:77] op_sel_hi:[1,0]
	s_waitcnt lgkmcnt(0)
	v_pk_fma_f32 v[92:93], v[4:5], v[82:83], v[86:87]
	v_pk_mul_f32 v[4:5], v[6:7], v[76:77] op_sel_hi:[1,0]
	v_pk_fma_f32 v[94:95], v[52:53], v[58:59], v[62:63]
	v_pk_fma_f32 v[96:97], v[4:5], v[84:85], v[88:89]
	v_cvt_pk_bf16_f32 v4, v90, v91
	v_cvt_pk_bf16_f32 v5, v94, v95
	v_cvt_pk_bf16_f32 v6, v92, v93
	v_cvt_pk_bf16_f32 v7, v96, v97
	ds_read_b128 v[52:55], v128
	ds_read_b128 v[56:59], v130
	global_store_dwordx4 v[172:173], v[4:7], off offset:128
	ds_read_b128 v[60:63], v129
	ds_read_b128 v[82:85], v131
	v_pk_mul_f32 v[50:51], v[50:51], v[76:77] op_sel_hi:[1,0]
	v_pk_mul_f32 v[8:9], v[8:9], v[76:77] op_sel_hi:[1,0]
	s_waitcnt lgkmcnt(2)
	v_pk_fma_f32 v[48:49], v[48:49], v[52:53], v[56:57]
	v_pk_fma_f32 v[52:53], v[50:51], v[54:55], v[58:59]
	s_waitcnt lgkmcnt(0)
	v_pk_fma_f32 v[50:51], v[8:9], v[60:61], v[82:83]
	v_pk_mul_f32 v[8:9], v[10:11], v[76:77] op_sel_hi:[1,0]
	v_cvt_pk_bf16_f32 v10, v50, v51
	v_pk_fma_f32 v[54:55], v[8:9], v[62:63], v[84:85]
	v_cvt_pk_bf16_f32 v8, v48, v49
	v_cvt_pk_bf16_f32 v9, v52, v53
	v_cvt_pk_bf16_f32 v11, v54, v55
	ds_read_b128 v[56:59], v132
	ds_read_b128 v[60:63], v134
	global_store_dwordx4 v[172:173], v[8:11], off offset:192
	ds_read_b128 v[82:85], v133
	ds_read_b128 v[86:89], v135
	v_pk_mul_f32 v[40:41], v[40:41], v[76:77] op_sel_hi:[1,0]
	v_pk_mul_f32 v[42:43], v[42:43], v[76:77] op_sel_hi:[1,0]
	v_pk_mul_f32 v[12:13], v[12:13], v[76:77] op_sel_hi:[1,0]
	s_waitcnt lgkmcnt(2)
	v_pk_fma_f32 v[40:41], v[40:41], v[56:57], v[60:61]
	v_pk_fma_f32 v[56:57], v[42:43], v[58:59], v[62:63]
	s_waitcnt lgkmcnt(0)
; #define LAS __attribute__((address_space(3)))
; __device__ __forceinline__ unsigned cvt_pk_bf16(float lo, float hi) { const bf16x2_t r = __builtin_convertvector((f32x2_t){lo, hi}, bf16x2_t); return __builtin_bit_cast(unsigned, r); }
; #define RT_LOAD(fr, c) do { _Pragma("unroll") for (int i = 0; i < 16; ++i) fr[i] = WFRAG((c) * 16 + i); } while (0)
; template <int MODE>
; __device__ __forceinline__ void norm_phase(const MkArgs& a, LAS unsigned char* lds, const int l, const int wv) {
;     ...
;         for (int j = 0; j < 8; ++j) {
;             const int k = 256 * w + 32 * j + 8 * q;
;             const f32x4 g0 = *(const LAS f32x4*)&tabA[k], g1 = *(const LAS f32x4*)&tabA[k + 4];
;             float gg[8] = {g0[0], g0[1], g0[2], g0[3], g1[0], g1[1], g1[2], g1[3]};
;             if constexpr (MODE != 3) {
;                 const f32x4 s0 = *(const LAS f32x4*)&tabB[k], s1 = *(const LAS f32x4*)&tabB[k + 4];
;                 const float sv[8] = {s0[0], s0[1], s0[2], s0[3], s1[0], s1[1], s1[2], s1[3]};
; #pragma unroll
;                 for (int i = 0; i < 8; ++i) xv[8 * j + i] = (xv[8 * j + i] * rstd) * gg[i] + sv[i];
;                 u32x4 o; o[0] = cvt_pk_bf16(xv[8 * j + 0], xv[8 * j + 1]); o[1] = cvt_pk_bf16(xv[8 * j + 2], xv[8 * j + 3]);
;                 o[2] = cvt_pk_bf16(xv[8 * j + 4], xv[8 * j + 5]); o[3] = cvt_pk_bf16(xv[8 * j + 6], xv[8 * j + 7]);
;                 *(u32x4*)(hb + (size_t)t * DM + k) = o;
;     ...
;             const char* wb = (const char*)(ws + WS_WRF) + ((size_t)l * 64 + w * 8) * 6 * 1024;
;             unsigned lo16 = (unsigned)lane * 16u; asm volatile("" : "+v"(lo16));
;     ...
;             f32x4 acc[3];
; #pragma unroll
;             for (int nt = 0; nt < 3; ++nt) acc[nt] = (f32x4){0.f, 0.f, 0.f, 0.f};
;             u32x4 frA[16], frB[16];
;     ...
;             RT_LOAD(frA, 0); RT_LOAD(frB, 1);
;             RT_MMA(frA, 0);
;             RT_LOAD(frA, 2);
;             RT_MMA(frB, 1);
;             RT_MMA(frA, 2);
	v_pk_fma_f32 v[42:43], v[12:13], v[82:83], v[86:87]
	v_pk_mul_f32 v[12:13], v[14:15], v[76:77] op_sel_hi:[1,0]
	v_cvt_pk_bf16_f32 v14, v42, v43
	v_pk_fma_f32 v[58:59], v[12:13], v[84:85], v[88:89]
	v_cvt_pk_bf16_f32 v12, v40, v41
	v_cvt_pk_bf16_f32 v13, v56, v57
	v_cvt_pk_bf16_f32 v15, v58, v59
	ds_read_b128 v[60:63], v136
	ds_read_b128 v[82:85], v138
	global_store_dwordx4 v[172:173], v[12:15], off offset:256
	ds_read_b128 v[86:89], v137
	ds_read_b128 v[160:163], v139
	v_pk_mul_f32 v[36:37], v[36:37], v[76:77] op_sel_hi:[1,0]
	v_pk_mul_f32 v[38:39], v[38:39], v[76:77] op_sel_hi:[1,0]
	v_pk_mul_f32 v[16:17], v[16:17], v[76:77] op_sel_hi:[1,0]
	s_waitcnt lgkmcnt(2)
	v_pk_fma_f32 v[36:37], v[36:37], v[60:61], v[82:83]
	v_pk_fma_f32 v[60:61], v[38:39], v[62:63], v[84:85]
	s_waitcnt lgkmcnt(0)
	v_pk_fma_f32 v[38:39], v[16:17], v[86:87], v[160:161]
	v_pk_mul_f32 v[16:17], v[18:19], v[76:77] op_sel_hi:[1,0]
	v_cvt_pk_bf16_f32 v18, v38, v39
	v_pk_fma_f32 v[62:63], v[16:17], v[88:89], v[162:163]
	v_cvt_pk_bf16_f32 v16, v36, v37
	v_cvt_pk_bf16_f32 v17, v60, v61
	v_cvt_pk_bf16_f32 v19, v62, v63
	ds_read_b128 v[82:85], v140
	ds_read_b128 v[86:89], v142
	global_store_dwordx4 v[172:173], v[16:19], off offset:320
	ds_read_b128 v[160:163], v141
	ds_read_b128 v[164:167], v143
	v_pk_mul_f32 v[32:33], v[32:33], v[76:77] op_sel_hi:[1,0]
	v_pk_mul_f32 v[34:35], v[34:35], v[76:77] op_sel_hi:[1,0]
	v_pk_mul_f32 v[20:21], v[20:21], v[76:77] op_sel_hi:[1,0]
	s_waitcnt lgkmcnt(2)
	v_pk_fma_f32 v[32:33], v[32:33], v[82:83], v[86:87]
	v_pk_fma_f32 v[82:83], v[34:35], v[84:85], v[88:89]
	s_waitcnt lgkmcnt(0)
	v_pk_fma_f32 v[34:35], v[20:21], v[160:161], v[164:165]
	v_pk_mul_f32 v[20:21], v[22:23], v[76:77] op_sel_hi:[1,0]
	v_cvt_pk_bf16_f32 v22, v34, v35
	v_pk_fma_f32 v[84:85], v[20:21], v[162:163], v[166:167]
	v_cvt_pk_bf16_f32 v20, v32, v33
	v_cvt_pk_bf16_f32 v21, v82, v83
	v_cvt_pk_bf16_f32 v23, v84, v85
	ds_read_b128 v[86:89], v144
	ds_read_b128 v[160:163], v146
	global_store_dwordx4 v[172:173], v[20:23], off offset:384
	ds_read_b128 v[164:167], v145
	ds_read_b128 v[168:171], v147
	v_pk_mul_f32 v[28:29], v[28:29], v[76:77] op_sel_hi:[1,0]
	v_pk_mul_f32 v[30:31], v[30:31], v[76:77] op_sel_hi:[1,0]
	v_pk_mul_f32 v[0:1], v[0:1], v[76:77] op_sel_hi:[1,0]
	s_waitcnt lgkmcnt(2)
	v_pk_fma_f32 v[28:29], v[28:29], v[86:87], v[160:161]
	v_pk_fma_f32 v[86:87], v[30:31], v[88:89], v[162:163]
	s_waitcnt lgkmcnt(0)
	v_pk_fma_f32 v[30:31], v[0:1], v[164:165], v[168:169]
	v_pk_mul_f32 v[0:1], v[2:3], v[76:77] op_sel_hi:[1,0]
	v_cvt_pk_bf16_f32 v2, v30, v31
	v_pk_fma_f32 v[88:89], v[0:1], v[166:167], v[170:171]
	v_cvt_pk_bf16_f32 v0, v28, v29
	v_cvt_pk_bf16_f32 v1, v86, v87
	v_cvt_pk_bf16_f32 v3, v88, v89
	v_mov_b32_e32 v76, v152
	global_store_dwordx4 v[172:173], v[0:3], off offset:448
	global_load_dwordx4 v[160:163], v76, s[22:23]
	global_load_dwordx4 v[164:167], v76, s[22:23] offset:1024
	global_load_dwordx4 v[168:171], v76, s[22:23] offset:2048
	global_load_dwordx4 v[172:175], v76, s[22:23] offset:3072
	s_add_u32 s12, s22, 0x1000
	s_addc_u32 s13, s23, 0
	global_load_dwordx4 v[176:179], v76, s[12:13]
	global_load_dwordx4 v[180:183], v76, s[12:13] offset:1024
	global_load_dwordx4 v[184:187], v76, s[12:13] offset:2048
	global_load_dwordx4 v[188:191], v76, s[12:13] offset:3072
	s_add_u32 s12, s22, 0x2000
	s_addc_u32 s13, s23, 0
	global_load_dwordx4 v[192:195], v76, s[12:13]
	global_load_dwordx4 v[196:199], v76, s[12:13] offset:1024
	global_load_dwordx4 v[200:203], v76, s[12:13] offset:2048
	global_load_dwordx4 v[204:207], v76, s[12:13] offset:3072
	s_add_u32 s12, s22, 0x3000
	s_addc_u32 s13, s23, 0
	global_load_dwordx4 v[208:211], v76, s[12:13]
	global_load_dwordx4 v[212:215], v76, s[12:13] offset:1024
	global_load_dwordx4 v[216:219], v76, s[12:13] offset:2048
	global_load_dwordx4 v[220:223], v76, s[12:13] offset:3072
	s_add_u32 s12, s22, 0x4000
	s_addc_u32 s13, s23, 0
	global_load_dwordx4 v[224:227], v76, s[12:13]
	global_load_dwordx4 v[228:231], v76, s[12:13] offset:1024
	v_lshlrev_b32_e32 v248, 16, v44
	v_and_b32_e32 v249, 0xffff0000, v44
	v_pk_add_f32 v[108:109], v[108:109], v[248:249] neg_lo:[0,1] neg_hi:[0,1]
	v_cvt_pk_bf16_f32 v244, v108, v109
	v_lshlrev_b32_e32 v250, 16, v45
	v_and_b32_e32 v251, 0xffff0000, v45
	v_pk_add_f32 v[112:113], v[112:113], v[250:251] neg_lo:[0,1] neg_hi:[0,1]
	v_cvt_pk_bf16_f32 v245, v112, v113
	v_lshlrev_b32_e32 v248, 16, v46
	v_and_b32_e32 v249, 0xffff0000, v46
	v_pk_add_f32 v[106:107], v[106:107], v[248:249] neg_lo:[0,1] neg_hi:[0,1]
	v_cvt_pk_bf16_f32 v246, v106, v107
	v_lshlrev_b32_e32 v250, 16, v47
	v_and_b32_e32 v251, 0xffff0000, v47
	v_pk_add_f32 v[110:111], v[110:111], v[250:251] neg_lo:[0,1] neg_hi:[0,1]
	v_cvt_pk_bf16_f32 v247, v110, v111
	s_waitcnt vmcnt(12)
	v_mfma_f32_16x16x32_bf16 v[232:235], v[44:47], v[160:163], 0
	v_mfma_f32_16x16x32_bf16 v[236:239], v[44:47], v[168:171], 0
	v_mfma_f32_16x16x32_bf16 v[240:243], v[44:47], v[176:179], 0
	v_mfma_f32_16x16x32_bf16 v[232:235], v[44:47], v[164:167], v[232:235]
	v_mfma_f32_16x16x32_bf16 v[236:239], v[44:47], v[172:175], v[236:239]
	v_mfma_f32_16x16x32_bf16 v[240:243], v[44:47], v[180:183], v[240:243]
	v_mfma_f32_16x16x32_bf16 v[232:235], v[244:247], v[160:163], v[232:235]
	v_mfma_f32_16x16x32_bf16 v[236:239], v[244:247], v[168:171], v[236:239]
	v_mfma_f32_16x16x32_bf16 v[240:243], v[244:247], v[176:179], v[240:243]
	global_load_dwordx4 v[160:163], v76, s[12:13] offset:2048
	global_load_dwordx4 v[164:167], v76, s[12:13] offset:3072
	s_add_u32 s12, s22, 0x5000
	s_addc_u32 s13, s23, 0
	global_load_dwordx4 v[168:171], v76, s[12:13]
	global_load_dwordx4 v[172:175], v76, s[12:13] offset:1024
	global_load_dwordx4 v[176:179], v76, s[12:13] offset:2048
	global_load_dwordx4 v[180:183], v76, s[12:13] offset:3072
	v_lshlrev_b32_e32 v248, 16, v24
	v_and_b32_e32 v249, 0xffff0000, v24
	v_pk_add_f32 v[98:99], v[98:99], v[248:249] neg_lo:[0,1] neg_hi:[0,1]
	v_cvt_pk_bf16_f32 v244, v98, v99
	v_lshlrev_b32_e32 v250, 16, v25
	v_and_b32_e32 v251, 0xffff0000, v25
	v_pk_add_f32 v[102:103], v[102:103], v[250:251] neg_lo:[0,1] neg_hi:[0,1]
	v_cvt_pk_bf16_f32 v245, v102, v103
	v_lshlrev_b32_e32 v248, 16, v26
	v_and_b32_e32 v249, 0xffff0000, v26
	v_pk_add_f32 v[100:101], v[100:101], v[248:249] neg_lo:[0,1] neg_hi:[0,1]
	v_cvt_pk_bf16_f32 v246, v100, v101
	v_lshlrev_b32_e32 v250, 16, v27
	v_and_b32_e32 v251, 0xffff0000, v27
	v_pk_add_f32 v[104:105], v[104:105], v[250:251] neg_lo:[0,1] neg_hi:[0,1]
	v_cvt_pk_bf16_f32 v247, v104, v105
	s_waitcnt vmcnt(12)
; #define RT_LOAD(fr, c) do { _Pragma("unroll") for (int i = 0; i < 16; ++i) fr[i] = WFRAG((c) * 16 + i); } while (0)
; template <int MODE>
; __device__ __forceinline__ void norm_phase(const MkArgs& a, LAS unsigned char* lds, const int l, const int wv) {
;     ...
;             RT_LOAD(frA, 0); RT_LOAD(frB, 1);
;             RT_MMA(frA, 0);
;             RT_LOAD(frA, 2);
;             RT_MMA(frB, 1);
;             RT_MMA(frA, 2);
	v_mfma_f32_16x16x32_bf16 v[232:235], v[24:27], v[184:187], v[232:235]
	v_mfma_f32_16x16x32_bf16 v[236:239], v[24:27], v[192:195], v[236:239]
	v_mfma_f32_16x16x32_bf16 v[240:243], v[24:27], v[200:203], v[240:243]
	v_mfma_f32_16x16x32_bf16 v[232:235], v[24:27], v[188:191], v[232:235]
	v_mfma_f32_16x16x32_bf16 v[236:239], v[24:27], v[196:199], v[236:239]
	v_mfma_f32_16x16x32_bf16 v[240:243], v[24:27], v[204:207], v[240:243]
	v_mfma_f32_16x16x32_bf16 v[232:235], v[244:247], v[184:187], v[232:235]
	v_mfma_f32_16x16x32_bf16 v[236:239], v[244:247], v[192:195], v[236:239]
	v_mfma_f32_16x16x32_bf16 v[240:243], v[244:247], v[200:203], v[240:243]
	s_add_u32 s12, s22, 0x6000
	s_addc_u32 s13, s23, 0
	global_load_dwordx4 v[184:187], v76, s[12:13]
	global_load_dwordx4 v[188:191], v76, s[12:13] offset:1024
	global_load_dwordx4 v[192:195], v76, s[12:13] offset:2048
	global_load_dwordx4 v[196:199], v76, s[12:13] offset:3072
	s_add_u32 s12, s22, 0x7000
	s_addc_u32 s13, s23, 0
	global_load_dwordx4 v[200:203], v76, s[12:13]
	global_load_dwordx4 v[204:207], v76, s[12:13] offset:1024
	v_lshlrev_b32_e32 v248, 16, v4
	v_and_b32_e32 v249, 0xffff0000, v4
	v_pk_add_f32 v[90:91], v[90:91], v[248:249] neg_lo:[0,1] neg_hi:[0,1]
	v_cvt_pk_bf16_f32 v244, v90, v91
	v_lshlrev_b32_e32 v250, 16, v5
	v_and_b32_e32 v251, 0xffff0000, v5
	v_pk_add_f32 v[94:95], v[94:95], v[250:251] neg_lo:[0,1] neg_hi:[0,1]
	v_cvt_pk_bf16_f32 v245, v94, v95
	v_lshlrev_b32_e32 v248, 16, v6
	v_and_b32_e32 v249, 0xffff0000, v6
	v_pk_add_f32 v[92:93], v[92:93], v[248:249] neg_lo:[0,1] neg_hi:[0,1]
	v_cvt_pk_bf16_f32 v246, v92, v93
	v_lshlrev_b32_e32 v250, 16, v7
	v_and_b32_e32 v251, 0xffff0000, v7
	v_pk_add_f32 v[96:97], v[96:97], v[250:251] neg_lo:[0,1] neg_hi:[0,1]
	v_cvt_pk_bf16_f32 v247, v96, v97
	s_waitcnt vmcnt(12)
	v_mfma_f32_16x16x32_bf16 v[232:235], v[4:7], v[208:211], v[232:235]
	v_mfma_f32_16x16x32_bf16 v[236:239], v[4:7], v[216:219], v[236:239]
	v_mfma_f32_16x16x32_bf16 v[240:243], v[4:7], v[224:227], v[240:243]
	v_mfma_f32_16x16x32_bf16 v[232:235], v[4:7], v[212:215], v[232:235]
	v_mfma_f32_16x16x32_bf16 v[236:239], v[4:7], v[220:223], v[236:239]
	v_mfma_f32_16x16x32_bf16 v[240:243], v[4:7], v[228:231], v[240:243]
	v_mfma_f32_16x16x32_bf16 v[232:235], v[244:247], v[208:211], v[232:235]
	v_mfma_f32_16x16x32_bf16 v[236:239], v[244:247], v[216:219], v[236:239]
	v_mfma_f32_16x16x32_bf16 v[240:243], v[244:247], v[224:227], v[240:243]
	global_load_dwordx4 v[208:211], v76, s[12:13] offset:2048
	global_load_dwordx4 v[212:215], v76, s[12:13] offset:3072
	s_add_u32 s12, s22, 0x8000
	s_addc_u32 s13, s23, 0
	global_load_dwordx4 v[216:219], v76, s[12:13]
	global_load_dwordx4 v[220:223], v76, s[12:13] offset:1024
	global_load_dwordx4 v[224:227], v76, s[12:13] offset:2048
	global_load_dwordx4 v[228:231], v76, s[12:13] offset:3072
	v_lshlrev_b32_e32 v248, 16, v8
	v_and_b32_e32 v249, 0xffff0000, v8
	v_pk_add_f32 v[48:49], v[48:49], v[248:249] neg_lo:[0,1] neg_hi:[0,1]
	v_cvt_pk_bf16_f32 v244, v48, v49
	v_lshlrev_b32_e32 v250, 16, v9
	v_and_b32_e32 v251, 0xffff0000, v9
	v_pk_add_f32 v[52:53], v[52:53], v[250:251] neg_lo:[0,1] neg_hi:[0,1]
	v_cvt_pk_bf16_f32 v245, v52, v53
	v_lshlrev_b32_e32 v248, 16, v10
	v_and_b32_e32 v249, 0xffff0000, v10
	v_pk_add_f32 v[50:51], v[50:51], v[248:249] neg_lo:[0,1] neg_hi:[0,1]
	v_cvt_pk_bf16_f32 v246, v50, v51
	v_lshlrev_b32_e32 v250, 16, v11
	v_and_b32_e32 v251, 0xffff0000, v11
	v_pk_add_f32 v[54:55], v[54:55], v[250:251] neg_lo:[0,1] neg_hi:[0,1]
	v_cvt_pk_bf16_f32 v247, v54, v55
	s_waitcnt vmcnt(12)
	v_mfma_f32_16x16x32_bf16 v[232:235], v[8:11], v[160:163], v[232:235]
	v_mfma_f32_16x16x32_bf16 v[236:239], v[8:11], v[168:171], v[236:239]
	v_mfma_f32_16x16x32_bf16 v[240:243], v[8:11], v[176:179], v[240:243]
	v_mfma_f32_16x16x32_bf16 v[232:235], v[8:11], v[164:167], v[232:235]
	v_mfma_f32_16x16x32_bf16 v[236:239], v[8:11], v[172:175], v[236:239]
	v_mfma_f32_16x16x32_bf16 v[240:243], v[8:11], v[180:183], v[240:243]
	v_mfma_f32_16x16x32_bf16 v[232:235], v[244:247], v[160:163], v[232:235]
	v_mfma_f32_16x16x32_bf16 v[236:239], v[244:247], v[168:171], v[236:239]
	v_mfma_f32_16x16x32_bf16 v[240:243], v[244:247], v[176:179], v[240:243]
	s_add_u32 s12, s22, 0x9000
	s_addc_u32 s13, s23, 0
	global_load_dwordx4 v[160:163], v76, s[12:13]
	global_load_dwordx4 v[164:167], v76, s[12:13] offset:1024
	global_load_dwordx4 v[168:171], v76, s[12:13] offset:2048
	global_load_dwordx4 v[172:175], v76, s[12:13] offset:3072
	s_add_u32 s12, s22, 0xa000
	s_addc_u32 s13, s23, 0
	global_load_dwordx4 v[176:179], v76, s[12:13]
	global_load_dwordx4 v[180:183], v76, s[12:13] offset:1024
	v_lshlrev_b32_e32 v248, 16, v12
	v_and_b32_e32 v249, 0xffff0000, v12
	v_pk_add_f32 v[40:41], v[40:41], v[248:249] neg_lo:[0,1] neg_hi:[0,1]
	v_cvt_pk_bf16_f32 v244, v40, v41
	v_lshlrev_b32_e32 v250, 16, v13
	v_and_b32_e32 v251, 0xffff0000, v13
	v_pk_add_f32 v[56:57], v[56:57], v[250:251] neg_lo:[0,1] neg_hi:[0,1]
	v_cvt_pk_bf16_f32 v245, v56, v57
	v_lshlrev_b32_e32 v248, 16, v14
	v_and_b32_e32 v249, 0xffff0000, v14
	v_pk_add_f32 v[42:43], v[42:43], v[248:249] neg_lo:[0,1] neg_hi:[0,1]
	v_cvt_pk_bf16_f32 v246, v42, v43
	v_lshlrev_b32_e32 v250, 16, v15
	v_and_b32_e32 v251, 0xffff0000, v15
	v_pk_add_f32 v[58:59], v[58:59], v[250:251] neg_lo:[0,1] neg_hi:[0,1]
	v_cvt_pk_bf16_f32 v247, v58, v59
	s_waitcnt vmcnt(12)
; #define RT_LOAD(fr, c) do { _Pragma("unroll") for (int i = 0; i < 16; ++i) fr[i] = WFRAG((c) * 16 + i); } while (0)
; template <int MODE>
; __device__ __forceinline__ void norm_phase(const MkArgs& a, LAS unsigned char* lds, const int l, const int wv) {
;     ...
;             RT_LOAD(frA, 0); RT_LOAD(frB, 1);
;             RT_MMA(frA, 0);
;             RT_LOAD(frA, 2);
;             RT_MMA(frB, 1);
;             RT_MMA(frA, 2);
;     ...
; #pragma unroll
;             for (int nt = 0; nt < 3; ++nt)
; #pragma unroll
;                 for (int e = 0; e < 4; ++e) part[(w * 16 + 4 * q + e) * 48 + 16 * nt + r] = acc[nt][e];
;     ...
;             __syncthreads();
	v_mfma_f32_16x16x32_bf16 v[232:235], v[12:15], v[184:187], v[232:235]
	v_mfma_f32_16x16x32_bf16 v[236:239], v[12:15], v[192:195], v[236:239]
	v_mfma_f32_16x16x32_bf16 v[240:243], v[12:15], v[200:203], v[240:243]
	v_mfma_f32_16x16x32_bf16 v[232:235], v[12:15], v[188:191], v[232:235]
	v_mfma_f32_16x16x32_bf16 v[236:239], v[12:15], v[196:199], v[236:239]
	v_mfma_f32_16x16x32_bf16 v[240:243], v[12:15], v[204:207], v[240:243]
	v_mfma_f32_16x16x32_bf16 v[232:235], v[244:247], v[184:187], v[232:235]
	v_mfma_f32_16x16x32_bf16 v[236:239], v[244:247], v[192:195], v[236:239]
	v_mfma_f32_16x16x32_bf16 v[240:243], v[244:247], v[200:203], v[240:243]
	global_load_dwordx4 v[184:187], v76, s[12:13] offset:2048
	global_load_dwordx4 v[188:191], v76, s[12:13] offset:3072
	s_add_u32 s12, s22, 0xb000
	s_addc_u32 s13, s23, 0
	global_load_dwordx4 v[192:195], v76, s[12:13]
	global_load_dwordx4 v[196:199], v76, s[12:13] offset:1024
	global_load_dwordx4 v[200:203], v76, s[12:13] offset:2048
	global_load_dwordx4 v[204:207], v76, s[12:13] offset:3072
	v_lshlrev_b32_e32 v248, 16, v16
	v_and_b32_e32 v249, 0xffff0000, v16
	v_pk_add_f32 v[36:37], v[36:37], v[248:249] neg_lo:[0,1] neg_hi:[0,1]
	v_cvt_pk_bf16_f32 v244, v36, v37
	v_lshlrev_b32_e32 v250, 16, v17
	v_and_b32_e32 v251, 0xffff0000, v17
	v_pk_add_f32 v[60:61], v[60:61], v[250:251] neg_lo:[0,1] neg_hi:[0,1]
	v_cvt_pk_bf16_f32 v245, v60, v61
	v_lshlrev_b32_e32 v248, 16, v18
	v_and_b32_e32 v249, 0xffff0000, v18
	v_pk_add_f32 v[38:39], v[38:39], v[248:249] neg_lo:[0,1] neg_hi:[0,1]
	v_cvt_pk_bf16_f32 v246, v38, v39
	v_lshlrev_b32_e32 v250, 16, v19
	v_and_b32_e32 v251, 0xffff0000, v19
	v_pk_add_f32 v[62:63], v[62:63], v[250:251] neg_lo:[0,1] neg_hi:[0,1]
	v_cvt_pk_bf16_f32 v247, v62, v63
	s_waitcnt vmcnt(12)
	v_mfma_f32_16x16x32_bf16 v[232:235], v[16:19], v[208:211], v[232:235]
	v_mfma_f32_16x16x32_bf16 v[236:239], v[16:19], v[216:219], v[236:239]
	v_mfma_f32_16x16x32_bf16 v[240:243], v[16:19], v[224:227], v[240:243]
	v_mfma_f32_16x16x32_bf16 v[232:235], v[16:19], v[212:215], v[232:235]
	v_mfma_f32_16x16x32_bf16 v[236:239], v[16:19], v[220:223], v[236:239]
	v_mfma_f32_16x16x32_bf16 v[240:243], v[16:19], v[228:231], v[240:243]
	v_mfma_f32_16x16x32_bf16 v[232:235], v[244:247], v[208:211], v[232:235]
	v_mfma_f32_16x16x32_bf16 v[236:239], v[244:247], v[216:219], v[236:239]
	v_mfma_f32_16x16x32_bf16 v[240:243], v[244:247], v[224:227], v[240:243]
	v_lshlrev_b32_e32 v248, 16, v20
	v_and_b32_e32 v249, 0xffff0000, v20
	v_pk_add_f32 v[32:33], v[32:33], v[248:249] neg_lo:[0,1] neg_hi:[0,1]
	v_cvt_pk_bf16_f32 v244, v32, v33
	v_lshlrev_b32_e32 v250, 16, v21
	v_and_b32_e32 v251, 0xffff0000, v21
	v_pk_add_f32 v[82:83], v[82:83], v[250:251] neg_lo:[0,1] neg_hi:[0,1]
	v_cvt_pk_bf16_f32 v245, v82, v83
	v_lshlrev_b32_e32 v248, 16, v22
	v_and_b32_e32 v249, 0xffff0000, v22
	v_pk_add_f32 v[34:35], v[34:35], v[248:249] neg_lo:[0,1] neg_hi:[0,1]
	v_cvt_pk_bf16_f32 v246, v34, v35
	v_lshlrev_b32_e32 v250, 16, v23
	v_and_b32_e32 v251, 0xffff0000, v23
	v_pk_add_f32 v[84:85], v[84:85], v[250:251] neg_lo:[0,1] neg_hi:[0,1]
	v_cvt_pk_bf16_f32 v247, v84, v85
	s_waitcnt vmcnt(6)
	v_mfma_f32_16x16x32_bf16 v[232:235], v[20:23], v[160:163], v[232:235]
	v_mfma_f32_16x16x32_bf16 v[236:239], v[20:23], v[168:171], v[236:239]
	v_mfma_f32_16x16x32_bf16 v[240:243], v[20:23], v[176:179], v[240:243]
	v_mfma_f32_16x16x32_bf16 v[232:235], v[20:23], v[164:167], v[232:235]
	v_mfma_f32_16x16x32_bf16 v[236:239], v[20:23], v[172:175], v[236:239]
	v_mfma_f32_16x16x32_bf16 v[240:243], v[20:23], v[180:183], v[240:243]
	v_mfma_f32_16x16x32_bf16 v[232:235], v[244:247], v[160:163], v[232:235]
	v_mfma_f32_16x16x32_bf16 v[236:239], v[244:247], v[168:171], v[236:239]
	v_mfma_f32_16x16x32_bf16 v[240:243], v[244:247], v[176:179], v[240:243]
	v_lshlrev_b32_e32 v248, 16, v0
	v_and_b32_e32 v249, 0xffff0000, v0
	v_pk_add_f32 v[28:29], v[28:29], v[248:249] neg_lo:[0,1] neg_hi:[0,1]
	v_cvt_pk_bf16_f32 v244, v28, v29
	v_lshlrev_b32_e32 v250, 16, v1
	v_and_b32_e32 v251, 0xffff0000, v1
	v_pk_add_f32 v[86:87], v[86:87], v[250:251] neg_lo:[0,1] neg_hi:[0,1]
	v_cvt_pk_bf16_f32 v245, v86, v87
	v_lshlrev_b32_e32 v248, 16, v2
	v_and_b32_e32 v249, 0xffff0000, v2
	v_pk_add_f32 v[30:31], v[30:31], v[248:249] neg_lo:[0,1] neg_hi:[0,1]
	v_cvt_pk_bf16_f32 v246, v30, v31
	v_lshlrev_b32_e32 v250, 16, v3
	v_and_b32_e32 v251, 0xffff0000, v3
	v_pk_add_f32 v[88:89], v[88:89], v[250:251] neg_lo:[0,1] neg_hi:[0,1]
	v_cvt_pk_bf16_f32 v247, v88, v89
	s_waitcnt vmcnt(0)
	v_mfma_f32_16x16x32_bf16 v[232:235], v[0:3], v[184:187], v[232:235]
	v_mfma_f32_16x16x32_bf16 v[236:239], v[0:3], v[192:195], v[236:239]
	v_mfma_f32_16x16x32_bf16 v[240:243], v[0:3], v[200:203], v[240:243]
	v_mfma_f32_16x16x32_bf16 v[232:235], v[0:3], v[188:191], v[232:235]
	v_mfma_f32_16x16x32_bf16 v[236:239], v[0:3], v[196:199], v[236:239]
	v_mfma_f32_16x16x32_bf16 v[240:243], v[0:3], v[204:207], v[240:243]
	v_mfma_f32_16x16x32_bf16 v[232:235], v[244:247], v[184:187], v[232:235]
	v_mfma_f32_16x16x32_bf16 v[236:239], v[244:247], v[192:195], v[236:239]
	v_mfma_f32_16x16x32_bf16 v[240:243], v[244:247], v[200:203], v[240:243]
	v_add_u32_e32 v4, 0x400, v156
	s_nop 7
	s_nop 1
	ds_write2_b32 v4, v232, v236 offset1:16
	ds_write2_b32 v4, v234, v238 offset0:96 offset1:112
	ds_write2_b32 v4, v240, v233 offset0:32 offset1:48
	ds_write2_b32 v4, v237, v241 offset0:64 offset1:80
	ds_write2_b32 v4, v242, v235 offset0:128 offset1:144
	ds_write2_b32 v4, v239, v243 offset0:160 offset1:176
	s_waitcnt lgkmcnt(0)
	s_barrier
	s_and_saveexec_b64 s[12:13], s[4:5]
	s_cbranch_execz .LBB0_904
	s_mov_b64 s[14:15], 0
	v_mov_b32_e32 v0, v114
	v_mov_b32_e32 v2, v64

; #define LAS __attribute__((address_space(3)))
; __device__ __forceinline__ unsigned cvt_pk_bf16(float lo, float hi) { const bf16x2_t r = __builtin_convertvector((f32x2_t){lo, hi}, bf16x2_t); return __builtin_bit_cast(unsigned, r); }
; template <int MODE>
; __device__ __forceinline__ void norm_phase(const MkArgs& a, LAS unsigned char* lds, const int l, const int wv) {
;     ...
;         __syncthreads();
;         float tot = 0.f;
; #pragma unroll
;         for (int i = 0; i < 8; ++i) tot += ssp[i * 16 + r];
;         const float rstd = 1.0f / sqrtf(tot * (1.0f / DM) + EPSV);
; #pragma unroll
;         for (int j = 0; j < 8; ++j) {
;             const int k = 256 * w + 32 * j + 8 * q;
;             const f32x4 g0 = *(const LAS f32x4*)&tabA[k], g1 = *(const LAS f32x4*)&tabA[k + 4];
;             float gg[8] = {g0[0], g0[1], g0[2], g0[3], g1[0], g1[1], g1[2], g1[3]};
;             if constexpr (MODE != 3) {
;                 const f32x4 s0 = *(const LAS f32x4*)&tabB[k], s1 = *(const LAS f32x4*)&tabB[k + 4];
;                 const float sv[8] = {s0[0], s0[1], s0[2], s0[3], s1[0], s1[1], s1[2], s1[3]};
; #pragma unroll
;                 for (int i = 0; i < 8; ++i) xv[8 * j + i] = (xv[8 * j + i] * rstd) * gg[i] + sv[i];
;                 u32x4 o; o[0] = cvt_pk_bf16(xv[8 * j + 0], xv[8 * j + 1]); o[1] = cvt_pk_bf16(xv[8 * j + 2], xv[8 * j + 3]);
;                 o[2] = cvt_pk_bf16(xv[8 * j + 4], xv[8 * j + 5]); o[3] = cvt_pk_bf16(xv[8 * j + 6], xv[8 * j + 7]);
;                 *(u32x4*)(hb + (size_t)t * DM + k) = o;
.LBB0_1973:
	s_or_b64 exec, exec, s[12:13]
	s_waitcnt lgkmcnt(0)
	s_barrier
	ds_read2_b32 v[84:85], v118 offset1:16
	ds_read2_b32 v[86:87], v118 offset0:32 offset1:48
	ds_read2_b32 v[88:89], v118 offset0:64 offset1:80
	s_mov_b32 s12, 0xf800000
	v_lshlrev_b64 v[82:83], 12, v[82:83]
	s_waitcnt lgkmcnt(2)
	v_add_f32_e32 v76, 0, v84
	v_add_f32_e32 v76, v76, v85
	ds_read2_b32 v[84:85], v118 offset0:96 offset1:112
	s_waitcnt lgkmcnt(2)
	v_add_f32_e32 v76, v76, v86
	v_add_f32_e32 v76, v76, v87
	s_waitcnt lgkmcnt(1)
	v_add_f32_e32 v76, v76, v88
	v_add_f32_e32 v76, v76, v89
	s_waitcnt lgkmcnt(0)
	v_add_f32_e32 v76, v76, v84
	v_add_f32_e32 v76, v76, v85
	v_fmamk_f32 v76, v76, 0x3a000000, v154
	v_mul_f32_e32 v84, 0x4f800000, v76
	v_cmp_gt_f32_e32 vcc, s12, v76
	v_lshl_add_u64 v[172:173], v[74:75], 0, v[82:83]
	s_nop 0
	v_cndmask_b32_e32 v76, v76, v84, vcc
	v_sqrt_f32_e32 v84, v76
	s_nop 0
	v_add_u32_e32 v85, -1, v84
	v_fma_f32 v86, -v85, v84, v76
	v_cmp_ge_f32_e64 s[12:13], 0, v86
	v_add_u32_e32 v86, 1, v84
	s_nop 0
	v_cndmask_b32_e64 v85, v84, v85, s[12:13]
	v_fma_f32 v84, -v86, v84, v76
	v_cmp_lt_f32_e64 s[12:13], 0, v84
	s_nop 1
	v_cndmask_b32_e64 v84, v85, v86, s[12:13]
	v_mul_f32_e32 v85, 0x37800000, v84
	v_cndmask_b32_e32 v84, v84, v85, vcc
	v_cmp_class_f32_e32 vcc, v76, v155
	s_nop 1
	v_cndmask_b32_e32 v76, v84, v76, vcc
	v_div_scale_f32 v84, s[12:13], v76, v76, 1.0
	v_rcp_f32_e32 v85, v84
	s_movk_i32 s12, 0x2000
	v_fma_f32 v86, -v84, v85, 1.0
	v_fmac_f32_e32 v85, v86, v85
	v_div_scale_f32 v86, vcc, 1.0, v76, 1.0
	v_mul_f32_e32 v87, v86, v85
	v_fma_f32 v88, -v84, v87, v86
	v_fmac_f32_e32 v87, v88, v85
	v_fma_f32 v84, -v84, v87, v86
	v_div_fmas_f32 v84, v84, v85, v87
	v_div_fixup_f32 v76, v84, v76, 1.0
	ds_read_b128 v[84:87], v65
	ds_read_b128 v[88:91], v124
	ds_read_b128 v[92:95], v123
	ds_read_b128 v[96:99], v125
	v_pk_mul_f32 v[60:61], v[60:61], v[76:77] op_sel_hi:[1,0]
	v_pk_mul_f32 v[44:45], v[44:45], v[76:77] op_sel_hi:[1,0]
	v_pk_mul_f32 v[56:57], v[56:57], v[76:77] op_sel_hi:[1,0]
	s_waitcnt lgkmcnt(2)
	v_pk_fma_f32 v[108:109], v[84:85], v[60:61], v[88:89]
	v_pk_mul_f32 v[60:61], v[62:63], v[76:77] op_sel_hi:[1,0]
	s_waitcnt lgkmcnt(0)
	v_pk_fma_f32 v[106:107], v[92:93], v[44:45], v[96:97]
	v_pk_mul_f32 v[44:45], v[46:47], v[76:77] op_sel_hi:[1,0]
	v_pk_fma_f32 v[112:113], v[86:87], v[60:61], v[90:91]
	v_pk_fma_f32 v[110:111], v[94:95], v[44:45], v[98:99]
	v_cvt_pk_bf16_f32 v44, v108, v109
	v_cvt_pk_bf16_f32 v45, v112, v113
	v_cvt_pk_bf16_f32 v46, v106, v107
	v_cvt_pk_bf16_f32 v47, v110, v111
	ds_read_b128 v[60:63], v126
	ds_read_b128 v[82:85], v128
	global_store_dwordx4 v[172:173], v[44:47], off
	ds_read_b128 v[86:89], v127
	ds_read_b128 v[90:93], v129
	v_pk_mul_f32 v[24:25], v[24:25], v[76:77] op_sel_hi:[1,0]
	v_pk_mul_f32 v[52:53], v[52:53], v[76:77] op_sel_hi:[1,0]
	s_waitcnt lgkmcnt(2)
	v_pk_fma_f32 v[98:99], v[56:57], v[60:61], v[82:83]
	v_pk_mul_f32 v[56:57], v[58:59], v[76:77] op_sel_hi:[1,0]
	s_waitcnt lgkmcnt(0)
	v_pk_fma_f32 v[100:101], v[24:25], v[86:87], v[90:91]
	v_pk_mul_f32 v[24:25], v[26:27], v[76:77] op_sel_hi:[1,0]
	v_pk_fma_f32 v[102:103], v[56:57], v[62:63], v[84:85]
	v_pk_fma_f32 v[104:105], v[24:25], v[88:89], v[92:93]
	v_cvt_pk_bf16_f32 v24, v98, v99
	v_cvt_pk_bf16_f32 v25, v102, v103
	v_cvt_pk_bf16_f32 v26, v100, v101
	v_cvt_pk_bf16_f32 v27, v104, v105
	ds_read_b128 v[56:59], v130
	ds_read_b128 v[60:63], v132
	global_store_dwordx4 v[172:173], v[24:27], off offset:64
	ds_read_b128 v[82:85], v131
	ds_read_b128 v[86:89], v133
	v_pk_mul_f32 v[4:5], v[4:5], v[76:77] op_sel_hi:[1,0]
	v_pk_mul_f32 v[48:49], v[48:49], v[76:77] op_sel_hi:[1,0]
	s_waitcnt lgkmcnt(2)
	v_pk_fma_f32 v[90:91], v[52:53], v[56:57], v[60:61]
	v_pk_mul_f32 v[52:53], v[54:55], v[76:77] op_sel_hi:[1,0]
	s_waitcnt lgkmcnt(0)
	v_pk_fma_f32 v[92:93], v[4:5], v[82:83], v[86:87]
	v_pk_mul_f32 v[4:5], v[6:7], v[76:77] op_sel_hi:[1,0]
	v_pk_fma_f32 v[94:95], v[52:53], v[58:59], v[62:63]
	v_pk_fma_f32 v[96:97], v[4:5], v[84:85], v[88:89]
	v_cvt_pk_bf16_f32 v4, v90, v91
	v_cvt_pk_bf16_f32 v5, v94, v95
	v_cvt_pk_bf16_f32 v6, v92, v93
	v_cvt_pk_bf16_f32 v7, v96, v97
	ds_read_b128 v[52:55], v134
	ds_read_b128 v[56:59], v136
	global_store_dwordx4 v[172:173], v[4:7], off offset:128
	ds_read_b128 v[60:63], v135
	ds_read_b128 v[82:85], v137
	v_pk_mul_f32 v[50:51], v[50:51], v[76:77] op_sel_hi:[1,0]
	v_pk_mul_f32 v[8:9], v[8:9], v[76:77] op_sel_hi:[1,0]
	s_waitcnt lgkmcnt(2)
	v_pk_fma_f32 v[48:49], v[48:49], v[52:53], v[56:57]
	v_pk_fma_f32 v[52:53], v[50:51], v[54:55], v[58:59]
	s_waitcnt lgkmcnt(0)
	v_pk_fma_f32 v[50:51], v[8:9], v[60:61], v[82:83]
	v_pk_mul_f32 v[8:9], v[10:11], v[76:77] op_sel_hi:[1,0]
	v_cvt_pk_bf16_f32 v10, v50, v51
	v_pk_fma_f32 v[54:55], v[8:9], v[62:63], v[84:85]
	v_cvt_pk_bf16_f32 v8, v48, v49
	v_cvt_pk_bf16_f32 v9, v52, v53
	v_cvt_pk_bf16_f32 v11, v54, v55
	ds_read_b128 v[56:59], v138
	ds_read_b128 v[60:63], v140
	global_store_dwordx4 v[172:173], v[8:11], off offset:192
	ds_read_b128 v[82:85], v139
	ds_read_b128 v[86:89], v141
	v_pk_mul_f32 v[40:41], v[40:41], v[76:77] op_sel_hi:[1,0]
	v_pk_mul_f32 v[42:43], v[42:43], v[76:77] op_sel_hi:[1,0]
	v_pk_mul_f32 v[12:13], v[12:13], v[76:77] op_sel_hi:[1,0]
	s_waitcnt lgkmcnt(2)
	v_pk_fma_f32 v[40:41], v[40:41], v[56:57], v[60:61]
	v_pk_fma_f32 v[56:57], v[42:43], v[58:59], v[62:63]
	s_waitcnt lgkmcnt(0)
; __device__ __forceinline__ unsigned cvt_pk_bf16(float lo, float hi) { const bf16x2_t r = __builtin_convertvector((f32x2_t){lo, hi}, bf16x2_t); return __builtin_bit_cast(unsigned, r); }
; #define RT_LOAD(fr, c) do { _Pragma("unroll") for (int i = 0; i < 16; ++i) fr[i] = WFRAG((c) * 16 + i); } while (0)
; template <int MODE>
; __device__ __forceinline__ void norm_phase(const MkArgs& a, LAS unsigned char* lds, const int l, const int wv) {
;     ...
;                 for (int i = 0; i < 8; ++i) xv[8 * j + i] = (xv[8 * j + i] * rstd) * gg[i] + sv[i];
;                 u32x4 o; o[0] = cvt_pk_bf16(xv[8 * j + 0], xv[8 * j + 1]); o[1] = cvt_pk_bf16(xv[8 * j + 2], xv[8 * j + 3]);
;                 o[2] = cvt_pk_bf16(xv[8 * j + 4], xv[8 * j + 5]); o[3] = cvt_pk_bf16(xv[8 * j + 6], xv[8 * j + 7]);
;                 *(u32x4*)(hb + (size_t)t * DM + k) = o;
;     ...
;             const char* wb = (const char*)(ws + WS_WRF) + ((size_t)l * 64 + w * 8) * 6 * 1024;
;             unsigned lo16 = (unsigned)lane * 16u; asm volatile("" : "+v"(lo16));
;     ...
;             f32x4 acc[3];
; #pragma unroll
;             for (int nt = 0; nt < 3; ++nt) acc[nt] = (f32x4){0.f, 0.f, 0.f, 0.f};
;             u32x4 frA[16], frB[16];
;     ...
;             RT_LOAD(frA, 0); RT_LOAD(frB, 1);
;             RT_MMA(frA, 0);
;             RT_LOAD(frA, 2);
;             RT_MMA(frB, 1);
;             RT_MMA(frA, 2);
	v_pk_fma_f32 v[42:43], v[12:13], v[82:83], v[86:87]
	v_pk_mul_f32 v[12:13], v[14:15], v[76:77] op_sel_hi:[1,0]
	v_cvt_pk_bf16_f32 v14, v42, v43
	v_pk_fma_f32 v[58:59], v[12:13], v[84:85], v[88:89]
	v_cvt_pk_bf16_f32 v12, v40, v41
	v_cvt_pk_bf16_f32 v13, v56, v57
	v_cvt_pk_bf16_f32 v15, v58, v59
	ds_read_b128 v[60:63], v142
	ds_read_b128 v[82:85], v144
	global_store_dwordx4 v[172:173], v[12:15], off offset:256
	ds_read_b128 v[86:89], v143
	ds_read_b128 v[160:163], v145
	v_pk_mul_f32 v[36:37], v[36:37], v[76:77] op_sel_hi:[1,0]
	v_pk_mul_f32 v[38:39], v[38:39], v[76:77] op_sel_hi:[1,0]
	v_pk_mul_f32 v[16:17], v[16:17], v[76:77] op_sel_hi:[1,0]
	s_waitcnt lgkmcnt(2)
	v_pk_fma_f32 v[36:37], v[36:37], v[60:61], v[82:83]
	v_pk_fma_f32 v[60:61], v[38:39], v[62:63], v[84:85]
	s_waitcnt lgkmcnt(0)
	v_pk_fma_f32 v[38:39], v[16:17], v[86:87], v[160:161]
	v_pk_mul_f32 v[16:17], v[18:19], v[76:77] op_sel_hi:[1,0]
	v_cvt_pk_bf16_f32 v18, v38, v39
	v_pk_fma_f32 v[62:63], v[16:17], v[88:89], v[162:163]
	v_cvt_pk_bf16_f32 v16, v36, v37
	v_cvt_pk_bf16_f32 v17, v60, v61
	v_cvt_pk_bf16_f32 v19, v62, v63
	ds_read_b128 v[82:85], v146
	ds_read_b128 v[86:89], v148
	global_store_dwordx4 v[172:173], v[16:19], off offset:320
	ds_read_b128 v[160:163], v147
	ds_read_b128 v[164:167], v149
	v_pk_mul_f32 v[32:33], v[32:33], v[76:77] op_sel_hi:[1,0]
	v_pk_mul_f32 v[34:35], v[34:35], v[76:77] op_sel_hi:[1,0]
	v_pk_mul_f32 v[20:21], v[20:21], v[76:77] op_sel_hi:[1,0]
	s_waitcnt lgkmcnt(2)
	v_pk_fma_f32 v[32:33], v[32:33], v[82:83], v[86:87]
	v_pk_fma_f32 v[82:83], v[34:35], v[84:85], v[88:89]
	s_waitcnt lgkmcnt(0)
	v_pk_fma_f32 v[34:35], v[20:21], v[160:161], v[164:165]
	v_pk_mul_f32 v[20:21], v[22:23], v[76:77] op_sel_hi:[1,0]
	v_cvt_pk_bf16_f32 v22, v34, v35
	v_pk_fma_f32 v[84:85], v[20:21], v[162:163], v[166:167]
	v_cvt_pk_bf16_f32 v20, v32, v33
	v_cvt_pk_bf16_f32 v21, v82, v83
	v_cvt_pk_bf16_f32 v23, v84, v85
	ds_read_b128 v[86:89], v150
	ds_read_b128 v[160:163], v152
	global_store_dwordx4 v[172:173], v[20:23], off offset:384
	ds_read_b128 v[164:167], v151
	ds_read_b128 v[168:171], v153
	v_pk_mul_f32 v[28:29], v[28:29], v[76:77] op_sel_hi:[1,0]
	v_pk_mul_f32 v[30:31], v[30:31], v[76:77] op_sel_hi:[1,0]
	v_pk_mul_f32 v[0:1], v[0:1], v[76:77] op_sel_hi:[1,0]
	s_waitcnt lgkmcnt(2)
	v_pk_fma_f32 v[28:29], v[28:29], v[86:87], v[160:161]
	v_pk_fma_f32 v[86:87], v[30:31], v[88:89], v[162:163]
	s_waitcnt lgkmcnt(0)
	v_pk_fma_f32 v[30:31], v[0:1], v[164:165], v[168:169]
	v_pk_mul_f32 v[0:1], v[2:3], v[76:77] op_sel_hi:[1,0]
	v_cvt_pk_bf16_f32 v2, v30, v31
	v_pk_fma_f32 v[88:89], v[0:1], v[166:167], v[170:171]
	v_cvt_pk_bf16_f32 v0, v28, v29
	v_cvt_pk_bf16_f32 v1, v86, v87
	v_cvt_pk_bf16_f32 v3, v88, v89
	v_mov_b32_e32 v76, v119
	global_store_dwordx4 v[172:173], v[0:3], off offset:448
	global_load_dwordx4 v[160:163], v76, s[22:23]
	global_load_dwordx4 v[164:167], v76, s[22:23] offset:1024
	global_load_dwordx4 v[168:171], v76, s[22:23] offset:2048
	global_load_dwordx4 v[172:175], v76, s[22:23] offset:3072
	s_add_u32 s12, s22, 0x1000
	s_addc_u32 s13, s23, 0
	global_load_dwordx4 v[176:179], v76, s[12:13]
	global_load_dwordx4 v[180:183], v76, s[12:13] offset:1024
	global_load_dwordx4 v[184:187], v76, s[12:13] offset:2048
	global_load_dwordx4 v[188:191], v76, s[12:13] offset:3072
	s_add_u32 s12, s22, 0x2000
	s_addc_u32 s13, s23, 0
	global_load_dwordx4 v[192:195], v76, s[12:13]
	global_load_dwordx4 v[196:199], v76, s[12:13] offset:1024
	global_load_dwordx4 v[200:203], v76, s[12:13] offset:2048
	global_load_dwordx4 v[204:207], v76, s[12:13] offset:3072
	s_add_u32 s12, s22, 0x3000
	s_addc_u32 s13, s23, 0
	global_load_dwordx4 v[208:211], v76, s[12:13]
	global_load_dwordx4 v[212:215], v76, s[12:13] offset:1024
	global_load_dwordx4 v[216:219], v76, s[12:13] offset:2048
	global_load_dwordx4 v[220:223], v76, s[12:13] offset:3072
	s_add_u32 s12, s22, 0x4000
	s_addc_u32 s13, s23, 0
	global_load_dwordx4 v[224:227], v76, s[12:13]
	global_load_dwordx4 v[228:231], v76, s[12:13] offset:1024
	v_lshlrev_b32_e32 v248, 16, v44
	v_and_b32_e32 v249, 0xffff0000, v44
	v_pk_add_f32 v[108:109], v[108:109], v[248:249] neg_lo:[0,1] neg_hi:[0,1]
	v_cvt_pk_bf16_f32 v244, v108, v109
	v_lshlrev_b32_e32 v250, 16, v45
	v_and_b32_e32 v251, 0xffff0000, v45
	v_pk_add_f32 v[112:113], v[112:113], v[250:251] neg_lo:[0,1] neg_hi:[0,1]
	v_cvt_pk_bf16_f32 v245, v112, v113
	v_lshlrev_b32_e32 v248, 16, v46
	v_and_b32_e32 v249, 0xffff0000, v46
	v_pk_add_f32 v[106:107], v[106:107], v[248:249] neg_lo:[0,1] neg_hi:[0,1]
	v_cvt_pk_bf16_f32 v246, v106, v107
	v_lshlrev_b32_e32 v250, 16, v47
	v_and_b32_e32 v251, 0xffff0000, v47
	v_pk_add_f32 v[110:111], v[110:111], v[250:251] neg_lo:[0,1] neg_hi:[0,1]
	v_cvt_pk_bf16_f32 v247, v110, v111
	s_waitcnt vmcnt(12)
	v_mfma_f32_16x16x32_bf16 v[232:235], v[44:47], v[160:163], 0
	v_mfma_f32_16x16x32_bf16 v[236:239], v[44:47], v[168:171], 0
	v_mfma_f32_16x16x32_bf16 v[240:243], v[44:47], v[176:179], 0
	v_mfma_f32_16x16x32_bf16 v[232:235], v[44:47], v[164:167], v[232:235]
	v_mfma_f32_16x16x32_bf16 v[236:239], v[44:47], v[172:175], v[236:239]
	v_mfma_f32_16x16x32_bf16 v[240:243], v[44:47], v[180:183], v[240:243]
	v_mfma_f32_16x16x32_bf16 v[232:235], v[244:247], v[160:163], v[232:235]
	v_mfma_f32_16x16x32_bf16 v[236:239], v[244:247], v[168:171], v[236:239]
	v_mfma_f32_16x16x32_bf16 v[240:243], v[244:247], v[176:179], v[240:243]
	global_load_dwordx4 v[160:163], v76, s[12:13] offset:2048
	global_load_dwordx4 v[164:167], v76, s[12:13] offset:3072
	s_add_u32 s12, s22, 0x5000
	s_addc_u32 s13, s23, 0
	global_load_dwordx4 v[168:171], v76, s[12:13]
	global_load_dwordx4 v[172:175], v76, s[12:13] offset:1024
	global_load_dwordx4 v[176:179], v76, s[12:13] offset:2048
	global_load_dwordx4 v[180:183], v76, s[12:13] offset:3072
	v_lshlrev_b32_e32 v248, 16, v24
	v_and_b32_e32 v249, 0xffff0000, v24
	v_pk_add_f32 v[98:99], v[98:99], v[248:249] neg_lo:[0,1] neg_hi:[0,1]
	v_cvt_pk_bf16_f32 v244, v98, v99
	v_lshlrev_b32_e32 v250, 16, v25
	v_and_b32_e32 v251, 0xffff0000, v25
	v_pk_add_f32 v[102:103], v[102:103], v[250:251] neg_lo:[0,1] neg_hi:[0,1]
	v_cvt_pk_bf16_f32 v245, v102, v103
	v_lshlrev_b32_e32 v248, 16, v26
	v_and_b32_e32 v249, 0xffff0000, v26
	v_pk_add_f32 v[100:101], v[100:101], v[248:249] neg_lo:[0,1] neg_hi:[0,1]
	v_cvt_pk_bf16_f32 v246, v100, v101
	v_lshlrev_b32_e32 v250, 16, v27
	v_and_b32_e32 v251, 0xffff0000, v27
	v_pk_add_f32 v[104:105], v[104:105], v[250:251] neg_lo:[0,1] neg_hi:[0,1]
	v_cvt_pk_bf16_f32 v247, v104, v105
	s_waitcnt vmcnt(12)
; #define RT_LOAD(fr, c) do { _Pragma("unroll") for (int i = 0; i < 16; ++i) fr[i] = WFRAG((c) * 16 + i); } while (0)
; template <int MODE>
; __device__ __forceinline__ void norm_phase(const MkArgs& a, LAS unsigned char* lds, const int l, const int wv) {
;     ...
;             RT_LOAD(frA, 0); RT_LOAD(frB, 1);
;             RT_MMA(frA, 0);
;             RT_LOAD(frA, 2);
;             RT_MMA(frB, 1);
;             RT_MMA(frA, 2);
	v_mfma_f32_16x16x32_bf16 v[232:235], v[24:27], v[184:187], v[232:235]
	v_mfma_f32_16x16x32_bf16 v[236:239], v[24:27], v[192:195], v[236:239]
	v_mfma_f32_16x16x32_bf16 v[240:243], v[24:27], v[200:203], v[240:243]
	v_mfma_f32_16x16x32_bf16 v[232:235], v[24:27], v[188:191], v[232:235]
	v_mfma_f32_16x16x32_bf16 v[236:239], v[24:27], v[196:199], v[236:239]
	v_mfma_f32_16x16x32_bf16 v[240:243], v[24:27], v[204:207], v[240:243]
	v_mfma_f32_16x16x32_bf16 v[232:235], v[244:247], v[184:187], v[232:235]
	v_mfma_f32_16x16x32_bf16 v[236:239], v[244:247], v[192:195], v[236:239]
	v_mfma_f32_16x16x32_bf16 v[240:243], v[244:247], v[200:203], v[240:243]
	s_add_u32 s12, s22, 0x6000
	s_addc_u32 s13, s23, 0
	global_load_dwordx4 v[184:187], v76, s[12:13]
	global_load_dwordx4 v[188:191], v76, s[12:13] offset:1024
	global_load_dwordx4 v[192:195], v76, s[12:13] offset:2048
	global_load_dwordx4 v[196:199], v76, s[12:13] offset:3072
	s_add_u32 s12, s22, 0x7000
	s_addc_u32 s13, s23, 0
	global_load_dwordx4 v[200:203], v76, s[12:13]
	global_load_dwordx4 v[204:207], v76, s[12:13] offset:1024
	v_lshlrev_b32_e32 v248, 16, v4
	v_and_b32_e32 v249, 0xffff0000, v4
	v_pk_add_f32 v[90:91], v[90:91], v[248:249] neg_lo:[0,1] neg_hi:[0,1]
	v_cvt_pk_bf16_f32 v244, v90, v91
	v_lshlrev_b32_e32 v250, 16, v5
	v_and_b32_e32 v251, 0xffff0000, v5
	v_pk_add_f32 v[94:95], v[94:95], v[250:251] neg_lo:[0,1] neg_hi:[0,1]
	v_cvt_pk_bf16_f32 v245, v94, v95
	v_lshlrev_b32_e32 v248, 16, v6
	v_and_b32_e32 v249, 0xffff0000, v6
	v_pk_add_f32 v[92:93], v[92:93], v[248:249] neg_lo:[0,1] neg_hi:[0,1]
	v_cvt_pk_bf16_f32 v246, v92, v93
	v_lshlrev_b32_e32 v250, 16, v7
	v_and_b32_e32 v251, 0xffff0000, v7
	v_pk_add_f32 v[96:97], v[96:97], v[250:251] neg_lo:[0,1] neg_hi:[0,1]
	v_cvt_pk_bf16_f32 v247, v96, v97
	s_waitcnt vmcnt(12)
	v_mfma_f32_16x16x32_bf16 v[232:235], v[4:7], v[208:211], v[232:235]
	v_mfma_f32_16x16x32_bf16 v[236:239], v[4:7], v[216:219], v[236:239]
	v_mfma_f32_16x16x32_bf16 v[240:243], v[4:7], v[224:227], v[240:243]
	v_mfma_f32_16x16x32_bf16 v[232:235], v[4:7], v[212:215], v[232:235]
	v_mfma_f32_16x16x32_bf16 v[236:239], v[4:7], v[220:223], v[236:239]
	v_mfma_f32_16x16x32_bf16 v[240:243], v[4:7], v[228:231], v[240:243]
	v_mfma_f32_16x16x32_bf16 v[232:235], v[244:247], v[208:211], v[232:235]
	v_mfma_f32_16x16x32_bf16 v[236:239], v[244:247], v[216:219], v[236:239]
	v_mfma_f32_16x16x32_bf16 v[240:243], v[244:247], v[224:227], v[240:243]
	global_load_dwordx4 v[208:211], v76, s[12:13] offset:2048
	global_load_dwordx4 v[212:215], v76, s[12:13] offset:3072
	s_add_u32 s12, s22, 0x8000
	s_addc_u32 s13, s23, 0
	global_load_dwordx4 v[216:219], v76, s[12:13]
	global_load_dwordx4 v[220:223], v76, s[12:13] offset:1024
	global_load_dwordx4 v[224:227], v76, s[12:13] offset:2048
	global_load_dwordx4 v[228:231], v76, s[12:13] offset:3072
	v_lshlrev_b32_e32 v248, 16, v8
	v_and_b32_e32 v249, 0xffff0000, v8
	v_pk_add_f32 v[48:49], v[48:49], v[248:249] neg_lo:[0,1] neg_hi:[0,1]
	v_cvt_pk_bf16_f32 v244, v48, v49
	v_lshlrev_b32_e32 v250, 16, v9
	v_and_b32_e32 v251, 0xffff0000, v9
	v_pk_add_f32 v[52:53], v[52:53], v[250:251] neg_lo:[0,1] neg_hi:[0,1]
	v_cvt_pk_bf16_f32 v245, v52, v53
	v_lshlrev_b32_e32 v248, 16, v10
	v_and_b32_e32 v249, 0xffff0000, v10
	v_pk_add_f32 v[50:51], v[50:51], v[248:249] neg_lo:[0,1] neg_hi:[0,1]
	v_cvt_pk_bf16_f32 v246, v50, v51
	v_lshlrev_b32_e32 v250, 16, v11
	v_and_b32_e32 v251, 0xffff0000, v11
	v_pk_add_f32 v[54:55], v[54:55], v[250:251] neg_lo:[0,1] neg_hi:[0,1]
	v_cvt_pk_bf16_f32 v247, v54, v55
	s_waitcnt vmcnt(12)
	v_mfma_f32_16x16x32_bf16 v[232:235], v[8:11], v[160:163], v[232:235]
	v_mfma_f32_16x16x32_bf16 v[236:239], v[8:11], v[168:171], v[236:239]
	v_mfma_f32_16x16x32_bf16 v[240:243], v[8:11], v[176:179], v[240:243]
	v_mfma_f32_16x16x32_bf16 v[232:235], v[8:11], v[164:167], v[232:235]
	v_mfma_f32_16x16x32_bf16 v[236:239], v[8:11], v[172:175], v[236:239]
	v_mfma_f32_16x16x32_bf16 v[240:243], v[8:11], v[180:183], v[240:243]
	v_mfma_f32_16x16x32_bf16 v[232:235], v[244:247], v[160:163], v[232:235]
	v_mfma_f32_16x16x32_bf16 v[236:239], v[244:247], v[168:171], v[236:239]
	v_mfma_f32_16x16x32_bf16 v[240:243], v[244:247], v[176:179], v[240:243]
	s_add_u32 s12, s22, 0x9000
	s_addc_u32 s13, s23, 0
	global_load_dwordx4 v[160:163], v76, s[12:13]
	global_load_dwordx4 v[164:167], v76, s[12:13] offset:1024
	global_load_dwordx4 v[168:171], v76, s[12:13] offset:2048
	global_load_dwordx4 v[172:175], v76, s[12:13] offset:3072
	s_add_u32 s12, s22, 0xa000
	s_addc_u32 s13, s23, 0
	global_load_dwordx4 v[176:179], v76, s[12:13]
	global_load_dwordx4 v[180:183], v76, s[12:13] offset:1024
	v_lshlrev_b32_e32 v248, 16, v12
	v_and_b32_e32 v249, 0xffff0000, v12
	v_pk_add_f32 v[40:41], v[40:41], v[248:249] neg_lo:[0,1] neg_hi:[0,1]
	v_cvt_pk_bf16_f32 v244, v40, v41
	v_lshlrev_b32_e32 v250, 16, v13
	v_and_b32_e32 v251, 0xffff0000, v13
	v_pk_add_f32 v[56:57], v[56:57], v[250:251] neg_lo:[0,1] neg_hi:[0,1]
	v_cvt_pk_bf16_f32 v245, v56, v57
	v_lshlrev_b32_e32 v248, 16, v14
	v_and_b32_e32 v249, 0xffff0000, v14
	v_pk_add_f32 v[42:43], v[42:43], v[248:249] neg_lo:[0,1] neg_hi:[0,1]
	v_cvt_pk_bf16_f32 v246, v42, v43
	v_lshlrev_b32_e32 v250, 16, v15
	v_and_b32_e32 v251, 0xffff0000, v15
	v_pk_add_f32 v[58:59], v[58:59], v[250:251] neg_lo:[0,1] neg_hi:[0,1]
	v_cvt_pk_bf16_f32 v247, v58, v59
	s_waitcnt vmcnt(12)
; #define RT_LOAD(fr, c) do { _Pragma("unroll") for (int i = 0; i < 16; ++i) fr[i] = WFRAG((c) * 16 + i); } while (0)
; template <int MODE>
; __device__ __forceinline__ void norm_phase(const MkArgs& a, LAS unsigned char* lds, const int l, const int wv) {
;     ...
;             RT_LOAD(frA, 0); RT_LOAD(frB, 1);
;             RT_MMA(frA, 0);
;             RT_LOAD(frA, 2);
;             RT_MMA(frB, 1);
;             RT_MMA(frA, 2);
;     ...
; #pragma unroll
;             for (int nt = 0; nt < 3; ++nt)
; #pragma unroll
;                 for (int e = 0; e < 4; ++e) part[(w * 16 + 4 * q + e) * 48 + 16 * nt + r] = acc[nt][e];
;     ...
;             __syncthreads();
	v_mfma_f32_16x16x32_bf16 v[232:235], v[12:15], v[184:187], v[232:235]
	v_mfma_f32_16x16x32_bf16 v[236:239], v[12:15], v[192:195], v[236:239]
	v_mfma_f32_16x16x32_bf16 v[240:243], v[12:15], v[200:203], v[240:243]
	v_mfma_f32_16x16x32_bf16 v[232:235], v[12:15], v[188:191], v[232:235]
	v_mfma_f32_16x16x32_bf16 v[236:239], v[12:15], v[196:199], v[236:239]
	v_mfma_f32_16x16x32_bf16 v[240:243], v[12:15], v[204:207], v[240:243]
	v_mfma_f32_16x16x32_bf16 v[232:235], v[244:247], v[184:187], v[232:235]
	v_mfma_f32_16x16x32_bf16 v[236:239], v[244:247], v[192:195], v[236:239]
	v_mfma_f32_16x16x32_bf16 v[240:243], v[244:247], v[200:203], v[240:243]
	global_load_dwordx4 v[184:187], v76, s[12:13] offset:2048
	global_load_dwordx4 v[188:191], v76, s[12:13] offset:3072
	s_add_u32 s12, s22, 0xb000
	s_addc_u32 s13, s23, 0
	global_load_dwordx4 v[192:195], v76, s[12:13]
	global_load_dwordx4 v[196:199], v76, s[12:13] offset:1024
	global_load_dwordx4 v[200:203], v76, s[12:13] offset:2048
	global_load_dwordx4 v[204:207], v76, s[12:13] offset:3072
	v_lshlrev_b32_e32 v248, 16, v16
	v_and_b32_e32 v249, 0xffff0000, v16
	v_pk_add_f32 v[36:37], v[36:37], v[248:249] neg_lo:[0,1] neg_hi:[0,1]
	v_cvt_pk_bf16_f32 v244, v36, v37
	v_lshlrev_b32_e32 v250, 16, v17
	v_and_b32_e32 v251, 0xffff0000, v17
	v_pk_add_f32 v[60:61], v[60:61], v[250:251] neg_lo:[0,1] neg_hi:[0,1]
	v_cvt_pk_bf16_f32 v245, v60, v61
	v_lshlrev_b32_e32 v248, 16, v18
	v_and_b32_e32 v249, 0xffff0000, v18
	v_pk_add_f32 v[38:39], v[38:39], v[248:249] neg_lo:[0,1] neg_hi:[0,1]
	v_cvt_pk_bf16_f32 v246, v38, v39
	v_lshlrev_b32_e32 v250, 16, v19
	v_and_b32_e32 v251, 0xffff0000, v19
	v_pk_add_f32 v[62:63], v[62:63], v[250:251] neg_lo:[0,1] neg_hi:[0,1]
	v_cvt_pk_bf16_f32 v247, v62, v63
	s_waitcnt vmcnt(12)
	v_mfma_f32_16x16x32_bf16 v[232:235], v[16:19], v[208:211], v[232:235]
	v_mfma_f32_16x16x32_bf16 v[236:239], v[16:19], v[216:219], v[236:239]
	v_mfma_f32_16x16x32_bf16 v[240:243], v[16:19], v[224:227], v[240:243]
	v_mfma_f32_16x16x32_bf16 v[232:235], v[16:19], v[212:215], v[232:235]
	v_mfma_f32_16x16x32_bf16 v[236:239], v[16:19], v[220:223], v[236:239]
	v_mfma_f32_16x16x32_bf16 v[240:243], v[16:19], v[228:231], v[240:243]
	v_mfma_f32_16x16x32_bf16 v[232:235], v[244:247], v[208:211], v[232:235]
	v_mfma_f32_16x16x32_bf16 v[236:239], v[244:247], v[216:219], v[236:239]
	v_mfma_f32_16x16x32_bf16 v[240:243], v[244:247], v[224:227], v[240:243]
	v_lshlrev_b32_e32 v248, 16, v20
	v_and_b32_e32 v249, 0xffff0000, v20
	v_pk_add_f32 v[32:33], v[32:33], v[248:249] neg_lo:[0,1] neg_hi:[0,1]
	v_cvt_pk_bf16_f32 v244, v32, v33
	v_lshlrev_b32_e32 v250, 16, v21
	v_and_b32_e32 v251, 0xffff0000, v21
	v_pk_add_f32 v[82:83], v[82:83], v[250:251] neg_lo:[0,1] neg_hi:[0,1]
	v_cvt_pk_bf16_f32 v245, v82, v83
	v_lshlrev_b32_e32 v248, 16, v22
	v_and_b32_e32 v249, 0xffff0000, v22
	v_pk_add_f32 v[34:35], v[34:35], v[248:249] neg_lo:[0,1] neg_hi:[0,1]
	v_cvt_pk_bf16_f32 v246, v34, v35
	v_lshlrev_b32_e32 v250, 16, v23
	v_and_b32_e32 v251, 0xffff0000, v23
	v_pk_add_f32 v[84:85], v[84:85], v[250:251] neg_lo:[0,1] neg_hi:[0,1]
	v_cvt_pk_bf16_f32 v247, v84, v85
	s_waitcnt vmcnt(6)
	v_mfma_f32_16x16x32_bf16 v[232:235], v[20:23], v[160:163], v[232:235]
	v_mfma_f32_16x16x32_bf16 v[236:239], v[20:23], v[168:171], v[236:239]
	v_mfma_f32_16x16x32_bf16 v[240:243], v[20:23], v[176:179], v[240:243]
	v_mfma_f32_16x16x32_bf16 v[232:235], v[20:23], v[164:167], v[232:235]
	v_mfma_f32_16x16x32_bf16 v[236:239], v[20:23], v[172:175], v[236:239]
	v_mfma_f32_16x16x32_bf16 v[240:243], v[20:23], v[180:183], v[240:243]
	v_mfma_f32_16x16x32_bf16 v[232:235], v[244:247], v[160:163], v[232:235]
	v_mfma_f32_16x16x32_bf16 v[236:239], v[244:247], v[168:171], v[236:239]
	v_mfma_f32_16x16x32_bf16 v[240:243], v[244:247], v[176:179], v[240:243]
	v_lshlrev_b32_e32 v248, 16, v0
	v_and_b32_e32 v249, 0xffff0000, v0
	v_pk_add_f32 v[28:29], v[28:29], v[248:249] neg_lo:[0,1] neg_hi:[0,1]
	v_cvt_pk_bf16_f32 v244, v28, v29
	v_lshlrev_b32_e32 v250, 16, v1
	v_and_b32_e32 v251, 0xffff0000, v1
	v_pk_add_f32 v[86:87], v[86:87], v[250:251] neg_lo:[0,1] neg_hi:[0,1]
	v_cvt_pk_bf16_f32 v245, v86, v87
	v_lshlrev_b32_e32 v248, 16, v2
	v_and_b32_e32 v249, 0xffff0000, v2
	v_pk_add_f32 v[30:31], v[30:31], v[248:249] neg_lo:[0,1] neg_hi:[0,1]
	v_cvt_pk_bf16_f32 v246, v30, v31
	v_lshlrev_b32_e32 v250, 16, v3
	v_and_b32_e32 v251, 0xffff0000, v3
	v_pk_add_f32 v[88:89], v[88:89], v[250:251] neg_lo:[0,1] neg_hi:[0,1]
	v_cvt_pk_bf16_f32 v247, v88, v89
	s_waitcnt vmcnt(0)
	v_mfma_f32_16x16x32_bf16 v[232:235], v[0:3], v[184:187], v[232:235]
	v_mfma_f32_16x16x32_bf16 v[236:239], v[0:3], v[192:195], v[236:239]
	v_mfma_f32_16x16x32_bf16 v[240:243], v[0:3], v[200:203], v[240:243]
	v_mfma_f32_16x16x32_bf16 v[232:235], v[0:3], v[188:191], v[232:235]
	v_mfma_f32_16x16x32_bf16 v[236:239], v[0:3], v[196:199], v[236:239]
	v_mfma_f32_16x16x32_bf16 v[240:243], v[0:3], v[204:207], v[240:243]
	v_mfma_f32_16x16x32_bf16 v[232:235], v[244:247], v[184:187], v[232:235]
	v_mfma_f32_16x16x32_bf16 v[236:239], v[244:247], v[192:195], v[236:239]
	v_mfma_f32_16x16x32_bf16 v[240:243], v[244:247], v[200:203], v[240:243]
	v_add_u32_e32 v4, 0x400, v156
	s_nop 7
	s_nop 1
	ds_write2_b32 v4, v232, v236 offset1:16
	ds_write2_b32 v4, v234, v238 offset0:96 offset1:112
	ds_write2_b32 v4, v240, v233 offset0:32 offset1:48
	ds_write2_b32 v4, v237, v241 offset0:64 offset1:80
	ds_write2_b32 v4, v242, v235 offset0:128 offset1:144
	ds_write2_b32 v4, v239, v243 offset0:160 offset1:176
	s_waitcnt lgkmcnt(0)
	s_barrier
	s_and_saveexec_b64 s[12:13], s[6:7]
	s_cbranch_execz .LBB0_1976
	s_mov_b64 s[14:15], 0
	v_mov_b32_e32 v0, v114
	v_mov_b32_e32 v2, v64
